# cache policy: P0 weight-transpose bf16 stores made non-temporal (streaming), loads were already nt
# baseline (speedup 1.0000x reference)
; __device__ __forceinline__ unsigned cvt_pk_bf16(float lo, float hi) { f32x2_t v = {lo, hi}; bf16x2_t b = __builtin_convertvector(v, bf16x2_t); return __builtin_bit_cast(unsigned, b); }
; #define LAS __attribute__((address_space(3)))
; __device__ __forceinline__ void tp_store(const TPItem& t, const f32x4 (&v)[16], const float2 (&gv)[8], LAS unsigned char* scr, int lane) {
;     const int nblk = t.N / 64, kb = t.idx / nblk, nb = t.idx - kb * nblk, k0 = 64 * kb, n0 = 64 * nb, kq = lane >> 4, p = lane & 15;
; #pragma unroll
;     for (int ii = 0; ii < 8; ++ii) { const float sa = gv[ii].x, sb = gv[ii].y;
; #pragma unroll
;         for (int j = 0; j < 4; ++j) { const int n = 4 * p + j;
;             *(LAS unsigned*)(scr + n * 128 + (((ii ^ (p & 7)) << 4) | (kq << 2))) = pg8::cvt_pk_bf16(v[2 * ii][j] * sa, v[2 * ii + 1][j] * sb); } }
.LBB0_28:
.LBB0_29:
	s_ashr_i32 s6, s31, 31
	s_lshr_b32 s6, s6, 26
	s_add_i32 s6, s31, s6
	s_ashr_i32 s6, s6, 6
	s_abs_i32 s20, s6
	v_cvt_f32_u32_e32 v141, s20
	v_mov_b32_e32 v188, v82
	v_mov_b32_e32 v189, v94
	v_pk_mul_f32 v[188:189], v[156:157], v[188:189]
	v_rcp_iflag_f32_e32 v141, v141
	s_sub_i32 s23, 0, s20
	s_abs_i32 s21, s30
	s_xor_b32 s22, s30, s6
	v_mul_f32_e32 v141, 0x4f7ffffe, v141
	v_cvt_u32_f32_e32 v141, v141
	s_ashr_i32 s22, s22, 31
	v_readfirstlane_b32 s24, v141
	v_cvt_pk_bf16_f32 v141, v188, v189
	v_mov_b32_e32 v188, v83
	v_mov_b32_e32 v189, v95
	v_pk_mul_f32 v[188:189], v[156:157], v[188:189]
	s_mul_i32 s23, s23, s24
	v_cvt_pk_bf16_f32 v187, v188, v189
	v_mov_b32_e32 v188, v84
	v_mov_b32_e32 v189, v96
	v_pk_mul_f32 v[188:189], v[156:157], v[188:189]
	ds_write2_b32 v172, v141, v187 offset1:32
	v_cvt_pk_bf16_f32 v141, v188, v189
	v_mov_b32_e32 v188, v85
	v_mov_b32_e32 v189, v97
	v_pk_mul_f32 v[188:189], v[156:157], v[188:189]
	s_mul_hi_u32 s23, s24, s23
	v_cvt_pk_bf16_f32 v187, v188, v189
	v_mov_b32_e32 v188, v106
	v_mov_b32_e32 v189, v66
	v_pk_mul_f32 v[188:189], v[158:159], v[188:189]
	ds_write2_b32 v172, v141, v187 offset0:64 offset1:96
	v_cvt_pk_bf16_f32 v141, v188, v189
	v_mov_b32_e32 v188, v107
	v_mov_b32_e32 v189, v67
	v_pk_mul_f32 v[188:189], v[158:159], v[188:189]
	s_add_i32 s24, s24, s23
	v_cvt_pk_bf16_f32 v187, v188, v189
	v_mov_b32_e32 v188, v108
	v_mov_b32_e32 v189, v68
	v_pk_mul_f32 v[188:189], v[158:159], v[188:189]
	ds_write2_b32 v173, v141, v187 offset1:32
	v_cvt_pk_bf16_f32 v141, v188, v189
	v_mov_b32_e32 v188, v109
	v_mov_b32_e32 v189, v69
	v_pk_mul_f32 v[188:189], v[158:159], v[188:189]
	s_mul_hi_u32 s23, s21, s24
	v_cvt_pk_bf16_f32 v187, v188, v189
	v_mov_b32_e32 v188, v70
	v_mov_b32_e32 v189, v74
	v_pk_mul_f32 v[188:189], v[160:161], v[188:189]
	ds_write2_b32 v173, v141, v187 offset0:64 offset1:96
	v_cvt_pk_bf16_f32 v141, v188, v189
	v_mov_b32_e32 v188, v71
	v_mov_b32_e32 v189, v75
	v_pk_mul_f32 v[188:189], v[160:161], v[188:189]
	s_mul_i32 s24, s23, s20
	v_cvt_pk_bf16_f32 v187, v188, v189
	v_mov_b32_e32 v188, v72
	v_mov_b32_e32 v189, v76
	v_pk_mul_f32 v[188:189], v[160:161], v[188:189]
	ds_write2_b32 v174, v141, v187 offset1:32
	v_cvt_pk_bf16_f32 v141, v188, v189
	v_mov_b32_e32 v188, v73
	v_mov_b32_e32 v189, v77
	v_pk_mul_f32 v[188:189], v[160:161], v[188:189]
	s_sub_i32 s21, s21, s24
	v_cvt_pk_bf16_f32 v187, v188, v189
	v_mov_b32_e32 v188, v78
	v_mov_b32_e32 v189, v86
	v_pk_mul_f32 v[188:189], v[162:163], v[188:189]
	ds_write2_b32 v174, v141, v187 offset0:64 offset1:96
	v_cvt_pk_bf16_f32 v141, v188, v189
	v_mov_b32_e32 v188, v79
	v_mov_b32_e32 v189, v87
	v_pk_mul_f32 v[188:189], v[162:163], v[188:189]
	s_add_i32 s25, s23, 1
	v_cvt_pk_bf16_f32 v187, v188, v189
	v_mov_b32_e32 v188, v80
	v_mov_b32_e32 v189, v88
	v_pk_mul_f32 v[188:189], v[162:163], v[188:189]
	ds_write2_b32 v175, v141, v187 offset1:32
	v_cvt_pk_bf16_f32 v141, v188, v189
	v_mov_b32_e32 v188, v81
	v_mov_b32_e32 v189, v89
	v_pk_mul_f32 v[188:189], v[162:163], v[188:189]
	s_sub_i32 s24, s21, s20
	v_cvt_pk_bf16_f32 v187, v188, v189
	v_mov_b32_e32 v188, v90
	v_mov_b32_e32 v189, v98
	v_pk_mul_f32 v[188:189], v[164:165], v[188:189]
	ds_write2_b32 v175, v141, v187 offset0:64 offset1:96
	v_cvt_pk_bf16_f32 v141, v188, v189
	v_mov_b32_e32 v188, v91
	v_mov_b32_e32 v189, v99
	v_pk_mul_f32 v[188:189], v[164:165], v[188:189]
	s_cmp_ge_u32 s21, s20
	v_cvt_pk_bf16_f32 v187, v188, v189
	v_mov_b32_e32 v188, v92
	v_mov_b32_e32 v189, v100
	v_pk_mul_f32 v[188:189], v[164:165], v[188:189]
	ds_write2_b32 v176, v141, v187 offset1:32
	v_cvt_pk_bf16_f32 v141, v188, v189
	v_mov_b32_e32 v188, v93
	v_mov_b32_e32 v189, v101
	v_pk_mul_f32 v[188:189], v[164:165], v[188:189]
	s_cselect_b32 s23, s25, s23
	v_cvt_pk_bf16_f32 v187, v188, v189
	v_mov_b32_e32 v188, v102
	v_mov_b32_e32 v189, v110
	v_pk_mul_f32 v[188:189], v[166:167], v[188:189]
	ds_write2_b32 v176, v141, v187 offset0:64 offset1:96
	v_cvt_pk_bf16_f32 v141, v188, v189
	v_mov_b32_e32 v188, v103
	v_mov_b32_e32 v189, v111
	v_pk_mul_f32 v[188:189], v[166:167], v[188:189]
	s_cselect_b32 s21, s24, s21
	v_cvt_pk_bf16_f32 v187, v188, v189
	v_mov_b32_e32 v188, v104
	v_mov_b32_e32 v189, v112
	v_pk_mul_f32 v[188:189], v[166:167], v[188:189]
	ds_write2_b32 v177, v141, v187 offset1:32
	v_cvt_pk_bf16_f32 v141, v188, v189
	v_mov_b32_e32 v188, v105
	v_mov_b32_e32 v189, v113
	v_pk_mul_f32 v[188:189], v[166:167], v[188:189]
	s_add_i32 s24, s23, 1
	v_cvt_pk_bf16_f32 v187, v188, v189
	v_mov_b32_e32 v188, v114
	v_mov_b32_e32 v189, v118
	v_pk_mul_f32 v[188:189], v[168:169], v[188:189]
	ds_write2_b32 v177, v141, v187 offset0:64 offset1:96
	v_cvt_pk_bf16_f32 v141, v188, v189
	v_mov_b32_e32 v188, v115
	v_mov_b32_e32 v189, v119
	v_pk_mul_f32 v[188:189], v[168:169], v[188:189]
	s_cmp_ge_u32 s21, s20
	v_cvt_pk_bf16_f32 v187, v188, v189
	v_mov_b32_e32 v188, v116
	v_mov_b32_e32 v189, v120
	v_pk_mul_f32 v[188:189], v[168:169], v[188:189]
	ds_write2_b32 v178, v141, v187 offset1:32
	v_cvt_pk_bf16_f32 v141, v188, v189
	v_mov_b32_e32 v188, v117
	v_mov_b32_e32 v189, v121
	v_pk_mul_f32 v[188:189], v[168:169], v[188:189]
	s_cselect_b32 s20, s24, s23
	v_cvt_pk_bf16_f32 v187, v188, v189
	v_mov_b32_e32 v188, v122
	v_mov_b32_e32 v189, v126
	v_pk_mul_f32 v[188:189], v[170:171], v[188:189]
	ds_write2_b32 v178, v141, v187 offset0:64 offset1:96
	v_cvt_pk_bf16_f32 v141, v188, v189
	v_mov_b32_e32 v188, v123
	v_mov_b32_e32 v189, v127
	v_pk_mul_f32 v[188:189], v[170:171], v[188:189]
	s_xor_b32 s20, s20, s22
	v_cvt_pk_bf16_f32 v187, v188, v189
	v_mov_b32_e32 v188, v124
	v_mov_b32_e32 v189, v128
	v_pk_mul_f32 v[188:189], v[170:171], v[188:189]
	s_sub_i32 s20, s20, s22
	ds_write2_b32 v179, v141, v187 offset1:32
	v_cvt_pk_bf16_f32 v141, v188, v189
	v_mov_b32_e32 v188, v125
	v_mov_b32_e32 v189, v129
	s_mul_i32 s6, s20, s6
	v_pk_mul_f32 v[188:189], v[170:171], v[188:189]
	s_sub_i32 s6, s30, s6
	v_cvt_pk_bf16_f32 v187, v188, v189
	ds_write2_b32 v179, v141, v187 offset0:64 offset1:96
	v_lshl_or_b32 v188, s6, 6, v137
	s_waitcnt lgkmcnt(0)
; #define LAS __attribute__((address_space(3)))
; #define GAS __attribute__((address_space(1)))
; #define WFENCE() asm volatile("s_waitcnt lgkmcnt(0)" ::: "memory")
; __device__ __forceinline__ void tp_store(const TPItem& t, const f32x4 (&v)[16], const float2 (&gv)[8], LAS unsigned char* scr, int lane) {
;     ...
;     const int c = lane & 7;
;     GAS bf16_t* dst = (GAS bf16_t*)(t.WT + (size_t)(n0 + (lane >> 3)) * t.K + k0 + 8 * c); const size_t dstep = (size_t)8 * t.K;
; #pragma unroll
;     for (int j = 0; j < 8; ++j) { const int n = (lane >> 3) + 8 * j; const u32x4 o = *(LAS const u32x4*)(scr + n * 128 + ((c ^ ((n >> 2) & 7)) << 4));
;         if (t.nt) __builtin_nontemporal_store(o, (GAS u32x4*)dst); else *(GAS u32x4*)dst = o;
;         dst += dstep; asm volatile("" : "+v"(dst)); }
;     WFENCE();
	v_ashrrev_i32_e32 v189, 31, v188
	v_lshlrev_b64 v[192:193], 13, v[188:189]
	ds_read_b128 v[188:191], v180
	s_lshl_b32 s20, s20, 6
	v_lshl_add_u64 v[192:193], s[18:19], 0, v[192:193]
	s_ashr_i32 s21, s20, 31
	v_lshl_add_u64 v[192:193], s[20:21], 1, v[192:193]
	v_lshl_add_u64 v[192:193], v[192:193], 0, v[134:135]
	s_waitcnt lgkmcnt(0)
	global_store_dwordx4 v[192:193], v[188:191], off nt
	v_lshl_add_u64 v[192:193], v[192:193], 0, s[16:17]
	ds_read_b128 v[188:191], v181
	s_cmpk_gt_i32 s26, 0x7bff
	s_cselect_b64 s[20:21], -1, 0
	s_waitcnt lgkmcnt(0)
	global_store_dwordx4 v[192:193], v[188:191], off nt
	v_lshl_add_u64 v[192:193], v[192:193], 0, s[16:17]
	ds_read_b128 v[188:191], v182
	s_waitcnt lgkmcnt(0)
	global_store_dwordx4 v[192:193], v[188:191], off nt
	v_lshl_add_u64 v[192:193], v[192:193], 0, s[16:17]
	ds_read_b128 v[188:191], v183
	s_waitcnt lgkmcnt(0)
	global_store_dwordx4 v[192:193], v[188:191], off nt
	v_lshl_add_u64 v[192:193], v[192:193], 0, s[16:17]
	ds_read_b128 v[188:191], v180 offset:4096
	s_waitcnt lgkmcnt(0)
	global_store_dwordx4 v[192:193], v[188:191], off nt
	v_lshl_add_u64 v[192:193], v[192:193], 0, s[16:17]
	ds_read_b128 v[188:191], v184
	s_waitcnt lgkmcnt(0)
	global_store_dwordx4 v[192:193], v[188:191], off nt
	v_lshl_add_u64 v[192:193], v[192:193], 0, s[16:17]
	ds_read_b128 v[188:191], v185
	s_waitcnt lgkmcnt(0)
	global_store_dwordx4 v[192:193], v[188:191], off nt
	v_lshl_add_u64 v[192:193], v[192:193], 0, s[16:17]
	ds_read_b128 v[188:191], v186
	s_waitcnt lgkmcnt(0)
	global_store_dwordx4 v[192:193], v[188:191], off nt
	s_nop 1
	v_lshl_add_u64 v[188:189], v[192:193], 0, s[16:17]
	s_waitcnt lgkmcnt(0)

; __device__ __forceinline__ unsigned cvt_pk_bf16(float lo, float hi) { f32x2_t v = {lo, hi}; bf16x2_t b = __builtin_convertvector(v, bf16x2_t); return __builtin_bit_cast(unsigned, b); }
; #define LAS __attribute__((address_space(3)))
; __device__ __forceinline__ void tp_store(const TPItem& t, const f32x4 (&v)[16], const float2 (&gv)[8], LAS unsigned char* scr, int lane) {
;     const int nblk = t.N / 64, kb = t.idx / nblk, nb = t.idx - kb * nblk, k0 = 64 * kb, n0 = 64 * nb, kq = lane >> 4, p = lane & 15;
; #pragma unroll
;     for (int ii = 0; ii < 8; ++ii) { const float sa = gv[ii].x, sb = gv[ii].y;
; #pragma unroll
;         for (int j = 0; j < 4; ++j) { const int n = 4 * p + j;
;             *(LAS unsigned*)(scr + n * 128 + (((ii ^ (p & 7)) << 4) | (kq << 2))) = pg8::cvt_pk_bf16(v[2 * ii][j] * sa, v[2 * ii + 1][j] * sb); } }
.LBB0_39:
.LBB0_40:
	s_ashr_i32 s6, s28, 31
	s_lshr_b32 s6, s6, 26
	s_add_i32 s6, s28, s6
	s_ashr_i32 s6, s6, 6
	s_abs_i32 s22, s6
	v_cvt_f32_u32_e32 v141, s22
	s_waitcnt vmcnt(15)
	v_mov_b32_e32 v188, v2
	s_waitcnt vmcnt(14)
	v_mov_b32_e32 v189, v6
	s_waitcnt vmcnt(7)
	v_pk_mul_f32 v[188:189], v[138:139], v[188:189]
	v_rcp_iflag_f32_e32 v141, v141
	s_sub_i32 s25, 0, s22
	s_abs_i32 s23, s11
	s_xor_b32 s24, s11, s6
	v_mul_f32_e32 v141, 0x4f7ffffe, v141
	v_cvt_u32_f32_e32 v141, v141
	s_ashr_i32 s24, s24, 31
	v_readfirstlane_b32 s26, v141
	v_cvt_pk_bf16_f32 v141, v188, v189
	v_mov_b32_e32 v188, v3
	v_mov_b32_e32 v189, v7
	v_pk_mul_f32 v[188:189], v[138:139], v[188:189]
	s_mul_i32 s25, s25, s26
	v_cvt_pk_bf16_f32 v187, v188, v189
	v_mov_b32_e32 v188, v4
	v_mov_b32_e32 v189, v8
	v_pk_mul_f32 v[188:189], v[138:139], v[188:189]
	ds_write2_b32 v172, v141, v187 offset1:32
	v_cvt_pk_bf16_f32 v141, v188, v189
	v_mov_b32_e32 v188, v5
	v_mov_b32_e32 v189, v9
	v_pk_mul_f32 v[188:189], v[138:139], v[188:189]
	s_mul_hi_u32 s25, s26, s25
	v_cvt_pk_bf16_f32 v187, v188, v189
	v_mov_b32_e32 v188, v10
	v_mov_b32_e32 v189, v14
	s_waitcnt vmcnt(6)
	v_pk_mul_f32 v[188:189], v[142:143], v[188:189]
	ds_write2_b32 v172, v141, v187 offset0:64 offset1:96
	v_cvt_pk_bf16_f32 v141, v188, v189
	v_mov_b32_e32 v188, v11
	v_mov_b32_e32 v189, v15
	v_pk_mul_f32 v[188:189], v[142:143], v[188:189]
	s_add_i32 s26, s26, s25
	v_cvt_pk_bf16_f32 v187, v188, v189
	v_mov_b32_e32 v188, v12
	v_mov_b32_e32 v189, v16
	v_pk_mul_f32 v[188:189], v[142:143], v[188:189]
	ds_write2_b32 v173, v141, v187 offset1:32
	v_cvt_pk_bf16_f32 v141, v188, v189
	v_mov_b32_e32 v188, v13
	v_mov_b32_e32 v189, v17
	v_pk_mul_f32 v[188:189], v[142:143], v[188:189]
	s_mul_hi_u32 s25, s23, s26
	v_cvt_pk_bf16_f32 v187, v188, v189
	v_mov_b32_e32 v188, v18
	v_mov_b32_e32 v189, v22
	s_waitcnt vmcnt(5)
	v_pk_mul_f32 v[188:189], v[144:145], v[188:189]
	ds_write2_b32 v173, v141, v187 offset0:64 offset1:96
	v_cvt_pk_bf16_f32 v141, v188, v189
	v_mov_b32_e32 v188, v19
	v_mov_b32_e32 v189, v23
	v_pk_mul_f32 v[188:189], v[144:145], v[188:189]
	s_mul_i32 s26, s25, s22
	v_cvt_pk_bf16_f32 v187, v188, v189
	v_mov_b32_e32 v188, v20
	v_mov_b32_e32 v189, v24
	v_pk_mul_f32 v[188:189], v[144:145], v[188:189]
	ds_write2_b32 v174, v141, v187 offset1:32
	v_cvt_pk_bf16_f32 v141, v188, v189
	v_mov_b32_e32 v188, v21
	v_mov_b32_e32 v189, v25
	v_pk_mul_f32 v[188:189], v[144:145], v[188:189]
	s_sub_i32 s23, s23, s26
	v_cvt_pk_bf16_f32 v187, v188, v189
	v_mov_b32_e32 v188, v26
	v_mov_b32_e32 v189, v30
	s_waitcnt vmcnt(4)
	v_pk_mul_f32 v[188:189], v[146:147], v[188:189]
	ds_write2_b32 v174, v141, v187 offset0:64 offset1:96
	v_cvt_pk_bf16_f32 v141, v188, v189
	v_mov_b32_e32 v188, v27
	v_mov_b32_e32 v189, v31
	v_pk_mul_f32 v[188:189], v[146:147], v[188:189]
	s_add_i32 s27, s25, 1
	v_cvt_pk_bf16_f32 v187, v188, v189
	v_mov_b32_e32 v188, v28
	v_mov_b32_e32 v189, v32
	v_pk_mul_f32 v[188:189], v[146:147], v[188:189]
	ds_write2_b32 v175, v141, v187 offset1:32
	v_cvt_pk_bf16_f32 v141, v188, v189
	v_mov_b32_e32 v188, v29
	v_mov_b32_e32 v189, v33
	v_pk_mul_f32 v[188:189], v[146:147], v[188:189]
	s_sub_i32 s26, s23, s22
	v_cvt_pk_bf16_f32 v187, v188, v189
	v_mov_b32_e32 v188, v34
	v_mov_b32_e32 v189, v38
	s_waitcnt vmcnt(3)
	v_pk_mul_f32 v[188:189], v[148:149], v[188:189]
	ds_write2_b32 v175, v141, v187 offset0:64 offset1:96
	v_cvt_pk_bf16_f32 v141, v188, v189
	v_mov_b32_e32 v188, v35
	v_mov_b32_e32 v189, v39
	v_pk_mul_f32 v[188:189], v[148:149], v[188:189]
	s_cmp_ge_u32 s23, s22
	v_cvt_pk_bf16_f32 v187, v188, v189
	v_mov_b32_e32 v188, v36
	v_mov_b32_e32 v189, v40
	v_pk_mul_f32 v[188:189], v[148:149], v[188:189]
	ds_write2_b32 v176, v141, v187 offset1:32
	v_cvt_pk_bf16_f32 v141, v188, v189
	v_mov_b32_e32 v188, v37
	v_mov_b32_e32 v189, v41
	v_pk_mul_f32 v[188:189], v[148:149], v[188:189]
	s_cselect_b32 s25, s27, s25
	v_cvt_pk_bf16_f32 v187, v188, v189
	v_mov_b32_e32 v188, v42
	v_mov_b32_e32 v189, v46
	s_waitcnt vmcnt(2)
; __device__ __forceinline__ unsigned cvt_pk_bf16(float lo, float hi) { f32x2_t v = {lo, hi}; bf16x2_t b = __builtin_convertvector(v, bf16x2_t); return __builtin_bit_cast(unsigned, b); }
; #define LAS __attribute__((address_space(3)))
; #define GAS __attribute__((address_space(1)))
; #define WFENCE() asm volatile("s_waitcnt lgkmcnt(0)" ::: "memory")
; __device__ __forceinline__ void tp_store(const TPItem& t, const f32x4 (&v)[16], const float2 (&gv)[8], LAS unsigned char* scr, int lane) {
;     ...
;     for (int ii = 0; ii < 8; ++ii) { const float sa = gv[ii].x, sb = gv[ii].y;
; #pragma unroll
;         for (int j = 0; j < 4; ++j) { const int n = 4 * p + j;
;             *(LAS unsigned*)(scr + n * 128 + (((ii ^ (p & 7)) << 4) | (kq << 2))) = pg8::cvt_pk_bf16(v[2 * ii][j] * sa, v[2 * ii + 1][j] * sb); } }
;     WFENCE();
;     const int c = lane & 7;
;     GAS bf16_t* dst = (GAS bf16_t*)(t.WT + (size_t)(n0 + (lane >> 3)) * t.K + k0 + 8 * c); const size_t dstep = (size_t)8 * t.K;
; #pragma unroll
;     for (int j = 0; j < 8; ++j) { const int n = (lane >> 3) + 8 * j; const u32x4 o = *(LAS const u32x4*)(scr + n * 128 + ((c ^ ((n >> 2) & 7)) << 4));
;         if (t.nt) __builtin_nontemporal_store(o, (GAS u32x4*)dst); else *(GAS u32x4*)dst = o;
;         dst += dstep; asm volatile("" : "+v"(dst)); }
;     WFENCE();
	v_pk_mul_f32 v[188:189], v[150:151], v[188:189]
	ds_write2_b32 v176, v141, v187 offset0:64 offset1:96
	v_cvt_pk_bf16_f32 v141, v188, v189
	v_mov_b32_e32 v188, v43
	v_mov_b32_e32 v189, v47
	v_pk_mul_f32 v[188:189], v[150:151], v[188:189]
	s_cselect_b32 s23, s26, s23
	v_cvt_pk_bf16_f32 v187, v188, v189
	v_mov_b32_e32 v188, v44
	v_mov_b32_e32 v189, v48
	v_pk_mul_f32 v[188:189], v[150:151], v[188:189]
	ds_write2_b32 v177, v141, v187 offset1:32
	v_cvt_pk_bf16_f32 v141, v188, v189
	v_mov_b32_e32 v188, v45
	v_mov_b32_e32 v189, v49
	v_pk_mul_f32 v[188:189], v[150:151], v[188:189]
	s_add_i32 s26, s25, 1
	v_cvt_pk_bf16_f32 v187, v188, v189
	v_mov_b32_e32 v188, v50
	v_mov_b32_e32 v189, v54
	s_waitcnt vmcnt(1)
	v_pk_mul_f32 v[188:189], v[152:153], v[188:189]
	ds_write2_b32 v177, v141, v187 offset0:64 offset1:96
	v_cvt_pk_bf16_f32 v141, v188, v189
	v_mov_b32_e32 v188, v51
	v_mov_b32_e32 v189, v55
	v_pk_mul_f32 v[188:189], v[152:153], v[188:189]
	s_cmp_ge_u32 s23, s22
	v_cvt_pk_bf16_f32 v187, v188, v189
	v_mov_b32_e32 v188, v52
	v_mov_b32_e32 v189, v56
	v_pk_mul_f32 v[188:189], v[152:153], v[188:189]
	ds_write2_b32 v178, v141, v187 offset1:32
	v_cvt_pk_bf16_f32 v141, v188, v189
	v_mov_b32_e32 v188, v53
	v_mov_b32_e32 v189, v57
	v_pk_mul_f32 v[188:189], v[152:153], v[188:189]
	s_cselect_b32 s22, s26, s25
	v_cvt_pk_bf16_f32 v187, v188, v189
	v_mov_b32_e32 v188, v58
	s_waitcnt vmcnt(0)
	v_mov_b32_e32 v189, v62
	v_pk_mul_f32 v[188:189], v[154:155], v[188:189]
	ds_write2_b32 v178, v141, v187 offset0:64 offset1:96
	v_cvt_pk_bf16_f32 v141, v188, v189
	v_mov_b32_e32 v188, v59
	v_mov_b32_e32 v189, v63
	v_pk_mul_f32 v[188:189], v[154:155], v[188:189]
	s_xor_b32 s22, s22, s24
	v_cvt_pk_bf16_f32 v187, v188, v189
	v_mov_b32_e32 v188, v60
	v_mov_b32_e32 v189, v64
	v_pk_mul_f32 v[188:189], v[154:155], v[188:189]
	s_sub_i32 s22, s22, s24
	ds_write2_b32 v179, v141, v187 offset1:32
	v_cvt_pk_bf16_f32 v141, v188, v189
	v_mov_b32_e32 v188, v61
	v_mov_b32_e32 v189, v65
	s_mul_i32 s6, s22, s6
	v_pk_mul_f32 v[188:189], v[154:155], v[188:189]
	s_sub_i32 s6, s11, s6
	v_cvt_pk_bf16_f32 v187, v188, v189
	ds_write2_b32 v179, v141, v187 offset0:64 offset1:96
	v_lshl_or_b32 v188, s6, 6, v137
	s_waitcnt lgkmcnt(0)
	v_ashrrev_i32_e32 v189, 31, v188
	v_lshlrev_b64 v[192:193], 13, v[188:189]
	ds_read_b128 v[188:191], v180
	s_lshl_b32 s22, s22, 6
	v_lshl_add_u64 v[192:193], s[4:5], 0, v[192:193]
	s_ashr_i32 s23, s22, 31
	v_lshl_add_u64 v[192:193], s[22:23], 1, v[192:193]
	v_lshl_add_u64 v[192:193], v[192:193], 0, v[134:135]
	s_waitcnt lgkmcnt(0)
	global_store_dwordx4 v[192:193], v[188:191], off nt
	v_lshl_add_u64 v[192:193], v[192:193], 0, s[16:17]
	ds_read_b128 v[188:191], v181
	s_andn2_b64 vcc, exec, s[20:21]
	s_mov_b64 s[20:21], -1
	s_waitcnt lgkmcnt(0)
	global_store_dwordx4 v[192:193], v[188:191], off nt
	v_lshl_add_u64 v[192:193], v[192:193], 0, s[16:17]
	ds_read_b128 v[188:191], v182
	s_waitcnt lgkmcnt(0)
	global_store_dwordx4 v[192:193], v[188:191], off nt
	v_lshl_add_u64 v[192:193], v[192:193], 0, s[16:17]
	ds_read_b128 v[188:191], v183
	s_waitcnt lgkmcnt(0)
	global_store_dwordx4 v[192:193], v[188:191], off nt
	v_lshl_add_u64 v[192:193], v[192:193], 0, s[16:17]
	ds_read_b128 v[188:191], v180 offset:4096
	s_waitcnt lgkmcnt(0)
	global_store_dwordx4 v[192:193], v[188:191], off nt
	v_lshl_add_u64 v[192:193], v[192:193], 0, s[16:17]
	ds_read_b128 v[188:191], v184
	s_waitcnt lgkmcnt(0)
	global_store_dwordx4 v[192:193], v[188:191], off nt
	v_lshl_add_u64 v[192:193], v[192:193], 0, s[16:17]
	ds_read_b128 v[188:191], v185
	s_waitcnt lgkmcnt(0)
	global_store_dwordx4 v[192:193], v[188:191], off nt
	v_lshl_add_u64 v[192:193], v[192:193], 0, s[16:17]
	ds_read_b128 v[188:191], v186
	s_waitcnt lgkmcnt(0)
	global_store_dwordx4 v[192:193], v[188:191], off nt
	s_nop 1
	v_lshl_add_u64 v[188:189], v[192:193], 0, s[16:17]
	s_waitcnt lgkmcnt(0)
	s_cbranch_vccnz .LBB0_30
	s_add_i32 s26, s34, s38
	s_add_i32 s6, s29, s33
	s_cmpk_gt_i32 s6, 0x7bff
	s_cbranch_scc1 .LBB0_29
	s_cmpk_gt_i32 s6, 0x73ff
	s_mov_b64 s[4:5], -1
	s_cbranch_scc0 .LBB0_44
	v_readlane_b32 s40, v252, 14
	v_readlane_b32 s48, v252, 22
	v_readlane_b32 s49, v252, 23
	v_readlane_b32 s50, v252, 24
	v_readlane_b32 s51, v252, 25
	s_mov_b64 s[24:25], s[50:51]
	s_mov_b64 s[20:21], s[48:49]
	s_add_i32 s11, s6, 0xffff8c00
	v_readlane_b32 s41, v252, 15
	v_readlane_b32 s42, v252, 16
	v_readlane_b32 s43, v252, 17
	v_readlane_b32 s44, v252, 18
	v_readlane_b32 s45, v252, 19
	v_readlane_b32 s46, v252, 20
	v_readlane_b32 s47, v252, 21
	v_readlane_b32 s52, v252, 26
	v_readlane_b32 s53, v252, 27
	v_readlane_b32 s54, v252, 28
	v_readlane_b32 s55, v252, 29
	s_mov_b64 s[4:5], 0
